# baseline (speedup 1.0000x reference)
.LBB5_134:
	s_or_b64 exec, exec, s[12:13]
	v_mov_b32_e32 v1, 0
	s_and_b64 vcc, exec, s[0:1]
	v_lshlrev_b32_e32 v131, 2, v131
	s_cbranch_vccnz .LBB5_138
	v_mov_b32_e32 v0, 0x23e90
	ds_read_b64 v[30:31], v0
	v_mov_b32_e32 v38, 0x3000
	v_lshl_or_b32 v165, v128, 4, v38
	v_mov_b32_e32 v38, 0x9000
	v_lshl_or_b32 v164, v128, 3, v38
	v_or_b32_e32 v166, 0x23900, v131
	v_lshlrev_b32_e32 v167, 2, v127
	v_or_b32_e32 v167, 0x23b00, v167
	v_mov_b32_e32 v94, 0xf149f2ca
	v_mov_b32_e32 v62, 0x3fb8aa3b
	v_mov_b32_e32 v63, 0x3fb8aa3b
	ds_read_b128 v[42:45], v166 offset:768
	ds_read_b128 v[50:53], v166 offset:832
	ds_read_b128 v[58:61], v166 offset:896
	ds_read_b128 v[66:69], v166 offset:960
	ds_read_b128 v[38:41], v166
	ds_read_b128 v[46:49], v166 offset:256
	ds_read_b128 v[132:135], v165
	ds_read_b128 v[136:139], v165 offset:1024
	ds_read_b128 v[140:143], v165 offset:8192
	ds_read_b128 v[144:147], v165 offset:9216
	s_waitcnt lgkmcnt(10)
	v_pk_add_f32 v[0:1], v[120:121], v[30:31] op_sel_hi:[1,0] neg_lo:[0,1] neg_hi:[0,1]
	v_pk_add_f32 v[32:33], v[122:123], v[30:31] op_sel_hi:[1,0] neg_lo:[0,1] neg_hi:[0,1]
	v_pk_mul_f32 v[0:1], v[30:31], v[0:1] op_sel:[1,0]
	v_pk_mul_f32 v[32:33], v[30:31], v[32:33] op_sel:[1,0]
	v_pk_fma_f32 v[84:85], v[70:71], v[0:1], v[102:103]
	v_pk_fma_f32 v[0:1], v[72:73], v[32:33], v[104:105]
	v_pk_add_f32 v[32:33], v[118:119], v[30:31] op_sel_hi:[1,0] neg_lo:[0,1] neg_hi:[0,1]
	v_pk_mul_f32 v[32:33], v[30:31], v[32:33] op_sel:[1,0]
	v_pk_fma_f32 v[118:119], v[74:75], v[32:33], v[106:107]
	v_pk_add_f32 v[32:33], v[124:125], v[30:31] op_sel_hi:[1,0] neg_lo:[0,1] neg_hi:[0,1]
	v_pk_mul_f32 v[32:33], v[30:31], v[32:33] op_sel:[1,0]
	v_pk_fma_f32 v[124:125], v[76:77], v[32:33], v[108:109]
	v_pk_add_f32 v[32:33], v[116:117], v[30:31] op_sel_hi:[1,0] neg_lo:[0,1] neg_hi:[0,1]
	v_pk_mul_f32 v[32:33], v[30:31], v[32:33] op_sel:[1,0]
	v_pk_fma_f32 v[116:117], v[96:97], v[32:33], v[86:87]
	v_pk_add_f32 v[32:33], v[114:115], v[30:31] op_sel_hi:[1,0] neg_lo:[0,1] neg_hi:[0,1]
	v_cvt_pk_bf16_f32 v34, v116, v117
	v_pk_mul_f32 v[32:33], v[30:31], v[32:33] op_sel:[1,0]
	v_cmp_eq_u32_e32 vcc, 3, v126
	v_pk_fma_f32 v[114:115], v[152:153], v[32:33], v[88:89]
	v_pk_add_f32 v[32:33], v[110:111], v[30:31] op_sel_hi:[1,0] neg_lo:[0,1] neg_hi:[0,1]
	v_cvt_pk_bf16_f32 v35, v114, v115
	v_pk_mul_f32 v[32:33], v[30:31], v[32:33] op_sel:[1,0]
	v_pk_fma_f32 v[110:111], v[90:91], v[32:33], v[98:99]
	v_pk_add_f32 v[32:33], v[112:113], v[30:31] op_sel_hi:[1,0] neg_lo:[0,1] neg_hi:[0,1]
	v_cvt_pk_bf16_f32 v36, v110, v111
	v_pk_mul_f32 v[30:31], v[30:31], v[32:33] op_sel:[1,0]
	v_cvt_pk_bf16_f32 v32, v118, v119
	v_pk_fma_f32 v[112:113], v[92:93], v[30:31], v[100:101]
	v_cvt_pk_bf16_f32 v30, v84, v85
	v_cvt_pk_bf16_f32 v31, v0, v1
	v_cvt_pk_bf16_f32 v33, v124, v125
	v_cvt_pk_bf16_f32 v37, v112, v113
	ds_read2_b32 v[54:55], v167 offset0:0 offset1:0
	ds_read2_b32 v[56:57], v167 offset0:0 offset1:0
	ds_read_b128 v[148:151], v165 offset:16384
	ds_read_b128 v[154:157], v165 offset:17408
	ds_read2st64_b64 v[96:99], v164 offset0:0 offset1:1
	ds_read2st64_b64 v[100:103], v164 offset0:4 offset1:5
	ds_read2st64_b64 v[104:107], v164 offset0:8 offset1:9
	ds_read2st64_b64 v[160:163], v164 offset0:12 offset1:13
	s_waitcnt lgkmcnt(4)
	v_mfma_f32_16x16x32_bf16 v[38:41], v[132:135], v[30:33], v[38:41]
	v_mfma_f32_16x16x32_bf16 v[46:49], v[140:143], v[30:33], v[46:49]
	v_mfma_f32_16x16x32_bf16 v[54:57], v[30:33], v[148:151], v[54:57]
	v_mfma_f32_16x16x32_bf16 v[38:41], v[136:139], v[34:37], v[38:41]
	v_mfma_f32_16x16x32_bf16 v[46:49], v[144:147], v[34:37], v[46:49]
	v_mfma_f32_16x16x32_bf16 v[54:57], v[34:37], v[154:157], v[54:57]
	ds_read_b128 v[132:135], v165 offset:2048
	ds_read_b128 v[136:139], v165 offset:3072
	ds_read_b128 v[140:143], v165 offset:10240
	ds_read_b128 v[144:147], v165 offset:11264
	ds_read_b128 v[148:151], v165 offset:18432
	ds_read_b128 v[154:157], v165 offset:19456
	s_nop 0
	v_cvt_pk_bf16_f32 v74, v38, v39
	v_cvt_pk_bf16_f32 v75, v40, v41
	v_cvt_pk_bf16_f32 v76, v46, v47
	v_cvt_pk_bf16_f32 v77, v48, v49
	ds_read_b128 v[38:41], v166 offset:64
	ds_read_b128 v[46:49], v166 offset:320
	v_mfma_f32_16x16x16_bf16 v[70:73], v[76:77], v[74:75], 0
	v_cvt_pk_bf16_f32 v86, v54, v55
	v_cvt_pk_bf16_f32 v87, v56, v57
	ds_read2_b32 v[54:55], v167 offset0:16 offset1:16
	ds_read2_b32 v[56:57], v167 offset0:16 offset1:16
	s_nop 3
	v_max_f32_e32 v88, v72, v73
	v_max3_f32 v88, v70, v71, v88
	v_cndmask_b32_e32 v88, v88, v94, vcc
	v_mov_b32_e32 v89, v88
	s_nop 1
	v_permlane16_swap_b32_e32 v88, v89
	v_max_f32_e32 v88, v88, v89
	v_mov_b32_e32 v89, v88
	s_nop 1
	v_permlane32_swap_b32_e32 v88, v89
	v_max_f32_e32 v88, v88, v89
	v_pk_add_f32 v[70:71], v[70:71], v[88:89] op_sel_hi:[1,0] neg_lo:[0,1] neg_hi:[0,1]
	v_pk_add_f32 v[72:73], v[72:73], v[88:89] op_sel_hi:[1,0] neg_lo:[0,1] neg_hi:[0,1]
	v_pk_mul_f32 v[70:71], v[62:63], v[70:71]
	v_pk_mul_f32 v[72:73], v[62:63], v[72:73]
	v_exp_f32_e32 v70, v70
	v_exp_f32_e32 v71, v71
	v_exp_f32_e32 v72, v72
	v_exp_f32_e32 v73, v73
	s_nop 0
	v_cndmask_b32_e64 v70, v70, 0, vcc
	v_cndmask_b32_e64 v71, v71, 0, vcc
	v_cndmask_b32_e64 v72, v72, 0, vcc
	v_cndmask_b32_e64 v73, v73, 0, vcc
	v_add_f32_e32 v90, v70, v71
	v_add_f32_e32 v91, v72, v73
	v_add_f32_e32 v90, v90, v91
	v_cvt_pk_bf16_f32 v92, v70, v71
	v_cvt_pk_bf16_f32 v93, v72, v73
	v_mov_b32_e32 v91, v90
	s_nop 1
	v_permlane16_swap_b32_e32 v90, v91
	v_add_f32_e32 v90, v90, v91
	v_mfma_f32_16x16x16_bf16 v[70:73], v[86:87], v[92:93], 0
	v_mov_b32_e32 v91, v90
	s_nop 1
	v_permlane32_swap_b32_e32 v90, v91
	v_add_f32_e32 v90, v90, v91
	v_rcp_f32_e32 v90, v90
	s_nop 2
	v_pk_mul_f32 v[70:71], v[70:71], v[90:91] op_sel_hi:[1,0]
	v_pk_mul_f32 v[72:73], v[72:73], v[90:91] op_sel_hi:[1,0]
	v_cvt_pk_bf16_f32 v120, v70, v71
	v_cvt_pk_bf16_f32 v121, v72, v73
	s_waitcnt lgkmcnt(0)
	v_mfma_f32_16x16x32_bf16 v[38:41], v[132:135], v[30:33], v[38:41]
	v_mfma_f32_16x16x32_bf16 v[46:49], v[140:143], v[30:33], v[46:49]
	v_mfma_f32_16x16x32_bf16 v[54:57], v[30:33], v[148:151], v[54:57]
	v_mfma_f32_16x16x32_bf16 v[38:41], v[136:139], v[34:37], v[38:41]
	v_mfma_f32_16x16x32_bf16 v[46:49], v[144:147], v[34:37], v[46:49]
	v_mfma_f32_16x16x32_bf16 v[54:57], v[34:37], v[154:157], v[54:57]
	ds_read_b128 v[132:135], v165 offset:4096
	ds_read_b128 v[136:139], v165 offset:5120
	ds_read_b128 v[140:143], v165 offset:12288
	ds_read_b128 v[144:147], v165 offset:13312
	ds_read_b128 v[148:151], v165 offset:20480
	ds_read_b128 v[154:157], v165 offset:21504
	s_nop 0
	v_cvt_pk_bf16_f32 v74, v38, v39
	v_cvt_pk_bf16_f32 v75, v40, v41
	v_cvt_pk_bf16_f32 v76, v46, v47
	v_cvt_pk_bf16_f32 v77, v48, v49
	ds_read_b128 v[38:41], v166 offset:128
	ds_read_b128 v[46:49], v166 offset:384
	v_mfma_f32_16x16x16_bf16 v[70:73], v[76:77], v[74:75], 0
	v_cvt_pk_bf16_f32 v86, v54, v55
	v_cvt_pk_bf16_f32 v87, v56, v57
	ds_read2_b32 v[54:55], v167 offset0:32 offset1:32
	ds_read2_b32 v[56:57], v167 offset0:32 offset1:32
	s_nop 3
	v_max_f32_e32 v88, v72, v73
	v_max3_f32 v88, v70, v71, v88
	v_cndmask_b32_e32 v88, v88, v94, vcc
	v_mov_b32_e32 v89, v88
	s_nop 1
	v_permlane16_swap_b32_e32 v88, v89
	v_max_f32_e32 v88, v88, v89
	v_mov_b32_e32 v89, v88
	s_nop 1
	v_permlane32_swap_b32_e32 v88, v89
	v_max_f32_e32 v88, v88, v89
	v_pk_add_f32 v[70:71], v[70:71], v[88:89] op_sel_hi:[1,0] neg_lo:[0,1] neg_hi:[0,1]
	v_pk_add_f32 v[72:73], v[72:73], v[88:89] op_sel_hi:[1,0] neg_lo:[0,1] neg_hi:[0,1]
	v_pk_mul_f32 v[70:71], v[62:63], v[70:71]
	v_pk_mul_f32 v[72:73], v[62:63], v[72:73]
	v_exp_f32_e32 v70, v70
	v_exp_f32_e32 v71, v71
	v_exp_f32_e32 v72, v72
	v_exp_f32_e32 v73, v73
	s_nop 0
	v_cndmask_b32_e64 v70, v70, 0, vcc
	v_cndmask_b32_e64 v71, v71, 0, vcc
	v_cndmask_b32_e64 v72, v72, 0, vcc
	v_cndmask_b32_e64 v73, v73, 0, vcc
	v_add_f32_e32 v90, v70, v71
	v_add_f32_e32 v91, v72, v73
	v_add_f32_e32 v90, v90, v91
	v_cvt_pk_bf16_f32 v92, v70, v71
	v_cvt_pk_bf16_f32 v93, v72, v73
	v_mov_b32_e32 v91, v90
	s_nop 1
	v_permlane16_swap_b32_e32 v90, v91
	v_add_f32_e32 v90, v90, v91
	v_mfma_f32_16x16x16_bf16 v[70:73], v[86:87], v[92:93], 0
	v_mov_b32_e32 v91, v90
	s_nop 1
	v_permlane32_swap_b32_e32 v90, v91
	v_add_f32_e32 v90, v90, v91
	v_rcp_f32_e32 v90, v90
	s_nop 2
	v_pk_mul_f32 v[70:71], v[70:71], v[90:91] op_sel_hi:[1,0]
	v_pk_mul_f32 v[72:73], v[72:73], v[90:91] op_sel_hi:[1,0]
	v_cvt_pk_bf16_f32 v122, v70, v71
	v_cvt_pk_bf16_f32 v123, v72, v73
	s_nop 1
	v_mfma_f32_16x16x32_bf16 v[42:45], v[96:99], v[120:123], v[42:45]
	v_mfma_f32_16x16x32_bf16 v[50:53], v[100:103], v[120:123], v[50:53]
	v_mfma_f32_16x16x32_bf16 v[58:61], v[104:107], v[120:123], v[58:61]
	v_mfma_f32_16x16x32_bf16 v[66:69], v[160:163], v[120:123], v[66:69]
	ds_read2st64_b64 v[96:99], v164 offset0:2 offset1:3
	ds_read2st64_b64 v[100:103], v164 offset0:6 offset1:7
	ds_read2st64_b64 v[104:107], v164 offset0:10 offset1:11
	ds_read2st64_b64 v[160:163], v164 offset0:14 offset1:15
	s_waitcnt lgkmcnt(4)
	v_mfma_f32_16x16x32_bf16 v[38:41], v[132:135], v[30:33], v[38:41]
	v_mfma_f32_16x16x32_bf16 v[46:49], v[140:143], v[30:33], v[46:49]
	v_mfma_f32_16x16x32_bf16 v[54:57], v[30:33], v[148:151], v[54:57]
	v_mfma_f32_16x16x32_bf16 v[38:41], v[136:139], v[34:37], v[38:41]
	v_mfma_f32_16x16x32_bf16 v[46:49], v[144:147], v[34:37], v[46:49]
	v_mfma_f32_16x16x32_bf16 v[54:57], v[34:37], v[154:157], v[54:57]
	ds_read_b128 v[132:135], v165 offset:6144
	ds_read_b128 v[136:139], v165 offset:7168
	ds_read_b128 v[140:143], v165 offset:14336
	ds_read_b128 v[144:147], v165 offset:15360
	ds_read_b128 v[148:151], v165 offset:22528
	ds_read_b128 v[154:157], v165 offset:23552
	s_nop 0
	v_cvt_pk_bf16_f32 v74, v38, v39
	v_cvt_pk_bf16_f32 v75, v40, v41
	v_cvt_pk_bf16_f32 v76, v46, v47
	v_cvt_pk_bf16_f32 v77, v48, v49
	ds_read_b128 v[38:41], v166 offset:192
	ds_read_b128 v[46:49], v166 offset:448
	v_mfma_f32_16x16x16_bf16 v[70:73], v[76:77], v[74:75], 0
	v_cvt_pk_bf16_f32 v86, v54, v55
	v_cvt_pk_bf16_f32 v87, v56, v57
	ds_read2_b32 v[54:55], v167 offset0:48 offset1:48
	ds_read2_b32 v[56:57], v167 offset0:48 offset1:48
	s_nop 3
	v_max_f32_e32 v88, v72, v73
	v_max3_f32 v88, v70, v71, v88
	v_cndmask_b32_e32 v88, v88, v94, vcc
	v_mov_b32_e32 v89, v88
	s_nop 1
	v_permlane16_swap_b32_e32 v88, v89
	v_max_f32_e32 v88, v88, v89
	v_mov_b32_e32 v89, v88
	s_nop 1
	v_permlane32_swap_b32_e32 v88, v89
	v_max_f32_e32 v88, v88, v89
	v_pk_add_f32 v[70:71], v[70:71], v[88:89] op_sel_hi:[1,0] neg_lo:[0,1] neg_hi:[0,1]
	v_pk_add_f32 v[72:73], v[72:73], v[88:89] op_sel_hi:[1,0] neg_lo:[0,1] neg_hi:[0,1]
	v_pk_mul_f32 v[70:71], v[62:63], v[70:71]
	v_pk_mul_f32 v[72:73], v[62:63], v[72:73]
	v_exp_f32_e32 v70, v70
	v_exp_f32_e32 v71, v71
	v_exp_f32_e32 v72, v72
	v_exp_f32_e32 v73, v73
	s_nop 0
	v_cndmask_b32_e64 v70, v70, 0, vcc
	v_cndmask_b32_e64 v71, v71, 0, vcc
	v_cndmask_b32_e64 v72, v72, 0, vcc
	v_cndmask_b32_e64 v73, v73, 0, vcc
	v_add_f32_e32 v90, v70, v71
	v_add_f32_e32 v91, v72, v73
	v_add_f32_e32 v90, v90, v91
	v_cvt_pk_bf16_f32 v92, v70, v71
	v_cvt_pk_bf16_f32 v93, v72, v73
	v_mov_b32_e32 v91, v90
	s_nop 1
	v_permlane16_swap_b32_e32 v90, v91
	v_add_f32_e32 v90, v90, v91
	v_mfma_f32_16x16x16_bf16 v[70:73], v[86:87], v[92:93], 0
	v_mov_b32_e32 v91, v90
	s_nop 1
	v_permlane32_swap_b32_e32 v90, v91
	v_add_f32_e32 v90, v90, v91
	v_rcp_f32_e32 v90, v90
	s_nop 2
	v_pk_mul_f32 v[70:71], v[70:71], v[90:91] op_sel_hi:[1,0]
	v_pk_mul_f32 v[72:73], v[72:73], v[90:91] op_sel_hi:[1,0]
	v_cvt_pk_bf16_f32 v120, v70, v71
	v_cvt_pk_bf16_f32 v121, v72, v73
	s_waitcnt lgkmcnt(0)
	v_mfma_f32_16x16x32_bf16 v[38:41], v[132:135], v[30:33], v[38:41]
	v_mfma_f32_16x16x32_bf16 v[46:49], v[140:143], v[30:33], v[46:49]
	v_mfma_f32_16x16x32_bf16 v[54:57], v[30:33], v[148:151], v[54:57]
	v_mfma_f32_16x16x32_bf16 v[38:41], v[136:139], v[34:37], v[38:41]
	v_mfma_f32_16x16x32_bf16 v[46:49], v[144:147], v[34:37], v[46:49]
	v_mfma_f32_16x16x32_bf16 v[54:57], v[34:37], v[154:157], v[54:57]
	s_nop 6
	v_cvt_pk_bf16_f32 v74, v38, v39
	v_cvt_pk_bf16_f32 v75, v40, v41
	v_cvt_pk_bf16_f32 v76, v46, v47
	v_cvt_pk_bf16_f32 v77, v48, v49
	s_nop 1
	v_mfma_f32_16x16x16_bf16 v[70:73], v[76:77], v[74:75], 0
	v_cvt_pk_bf16_f32 v86, v54, v55
	v_cvt_pk_bf16_f32 v87, v56, v57
	s_nop 5
	v_max_f32_e32 v88, v72, v73
	v_max3_f32 v88, v70, v71, v88
	v_cndmask_b32_e32 v88, v88, v94, vcc
	v_mov_b32_e32 v89, v88
	s_nop 1
	v_permlane16_swap_b32_e32 v88, v89
	v_max_f32_e32 v88, v88, v89
	v_mov_b32_e32 v89, v88
	s_nop 1
	v_permlane32_swap_b32_e32 v88, v89
	v_max_f32_e32 v88, v88, v89
	v_pk_add_f32 v[70:71], v[70:71], v[88:89] op_sel_hi:[1,0] neg_lo:[0,1] neg_hi:[0,1]
	v_pk_add_f32 v[72:73], v[72:73], v[88:89] op_sel_hi:[1,0] neg_lo:[0,1] neg_hi:[0,1]
	v_pk_mul_f32 v[70:71], v[62:63], v[70:71]
	v_pk_mul_f32 v[72:73], v[62:63], v[72:73]
	v_exp_f32_e32 v70, v70
	v_exp_f32_e32 v71, v71
	v_exp_f32_e32 v72, v72
	v_exp_f32_e32 v73, v73
	s_nop 0
	v_cndmask_b32_e64 v70, v70, 0, vcc
	v_cndmask_b32_e64 v71, v71, 0, vcc
	v_cndmask_b32_e64 v72, v72, 0, vcc
	v_cndmask_b32_e64 v73, v73, 0, vcc
	v_add_f32_e32 v90, v70, v71
	v_add_f32_e32 v91, v72, v73
	v_add_f32_e32 v90, v90, v91
	v_cvt_pk_bf16_f32 v92, v70, v71
	v_cvt_pk_bf16_f32 v93, v72, v73
	v_mov_b32_e32 v91, v90
	s_nop 1
	v_permlane16_swap_b32_e32 v90, v91
	v_add_f32_e32 v90, v90, v91
	v_mfma_f32_16x16x16_bf16 v[70:73], v[86:87], v[92:93], 0
	v_mov_b32_e32 v91, v90
	s_nop 1
	v_permlane32_swap_b32_e32 v90, v91
	v_add_f32_e32 v90, v90, v91
	v_rcp_f32_e32 v90, v90
	s_nop 2
	v_pk_mul_f32 v[70:71], v[70:71], v[90:91] op_sel_hi:[1,0]
	v_pk_mul_f32 v[72:73], v[72:73], v[90:91] op_sel_hi:[1,0]
	v_cvt_pk_bf16_f32 v122, v70, v71
	v_cvt_pk_bf16_f32 v123, v72, v73
	s_nop 1
	v_mfma_f32_16x16x32_bf16 v[42:45], v[96:99], v[120:123], v[42:45]
	v_mfma_f32_16x16x32_bf16 v[50:53], v[100:103], v[120:123], v[50:53]
	v_mfma_f32_16x16x32_bf16 v[58:61], v[104:107], v[120:123], v[58:61]
	v_mfma_f32_16x16x32_bf16 v[66:69], v[160:163], v[120:123], v[66:69]
	s_nop 1
	s_nop 3
	v_pk_add_f32 v[120:121], v[42:43], v[84:85]
	v_pk_add_f32 v[122:123], v[44:45], v[0:1]
	v_mul_f32_e32 v1, v130, v120
	v_mul_f32_e32 v0, v120, v1
	v_mul_f32_e32 v31, v130, v121
	v_pk_add_f32 v[0:1], v[0:1], 0 op_sel_hi:[1,0]
	v_mul_f32_e32 v30, v121, v31
	v_pk_add_f32 v[0:1], v[0:1], v[30:31]
	v_mul_f32_e32 v31, v130, v122
	v_mul_f32_e32 v30, v122, v31
	v_pk_add_f32 v[0:1], v[0:1], v[30:31]
	v_mul_f32_e32 v31, v130, v123
	v_pk_add_f32 v[118:119], v[50:51], v[118:119]
	v_mul_f32_e32 v30, v123, v31
	v_pk_add_f32 v[0:1], v[0:1], v[30:31]
	v_mul_f32_e32 v31, v130, v118
	v_mul_f32_e32 v30, v118, v31
	v_pk_add_f32 v[124:125], v[52:53], v[124:125]
	v_pk_add_f32 v[0:1], v[0:1], v[30:31]
	v_mul_f32_e32 v31, v130, v119
	v_mul_f32_e32 v30, v119, v31
	v_mul_f32_e32 v33, v130, v124
	v_pk_add_f32 v[116:117], v[58:59], v[116:117]
	v_mul_f32_e32 v32, v124, v33
	v_mul_f32_e32 v35, v130, v125
	v_pk_add_f32 v[0:1], v[0:1], v[30:31]
	v_mul_f32_e32 v34, v125, v35
	v_mul_f32_e32 v37, v130, v116
	v_pk_add_f32 v[0:1], v[0:1], v[32:33]
	v_pk_add_f32 v[114:115], v[60:61], v[114:115]
	v_mul_f32_e32 v36, v116, v37
	v_mul_f32_e32 v39, v130, v117
	v_pk_add_f32 v[0:1], v[0:1], v[34:35]
	v_mul_f32_e32 v38, v117, v39
	v_mul_f32_e32 v41, v130, v114
	v_pk_add_f32 v[0:1], v[0:1], v[36:37]
	v_pk_add_f32 v[110:111], v[66:67], v[110:111]
	v_mul_f32_e32 v40, v114, v41
	v_mul_f32_e32 v43, v130, v115
	v_pk_add_f32 v[0:1], v[0:1], v[38:39]
	v_mul_f32_e32 v42, v115, v43
	v_mul_f32_e32 v45, v130, v110
	v_pk_add_f32 v[0:1], v[0:1], v[40:41]
	v_pk_add_f32 v[112:113], v[68:69], v[112:113]
	v_mul_f32_e32 v44, v110, v45
	v_mul_f32_e32 v47, v130, v111
	v_pk_add_f32 v[0:1], v[0:1], v[42:43]
	v_mul_f32_e32 v46, v111, v47
	v_mul_f32_e32 v49, v130, v112
	v_pk_add_f32 v[0:1], v[0:1], v[44:45]
	v_mul_f32_e32 v48, v112, v49
	v_pk_add_f32 v[0:1], v[0:1], v[46:47]
	v_mul_f32_e32 v31, v130, v113
	v_pk_add_f32 v[0:1], v[0:1], v[48:49]
	v_mul_f32_e32 v30, v113, v31
	v_pk_add_f32 v[0:1], v[0:1], v[30:31]
	s_branch .LBB5_139
